# baseline (speedup 1.0000x reference)
_Z7gemm128ILi1ELi96EEv8GemmArgs:
	s_cmp_lt_u32 s2, 0x100
	s_cbranch_scc1 .Lou_body
	s_endpgm
.Lou_body:
	s_load_dwordx4 s[4:7], s[0:1], 0x0
	s_load_dwordx2 s[8:9], s[0:1], 0x20
	s_load_dwordx2 s[10:11], s[0:1], 0x38
	s_load_dwordx2 s[24:25], s[0:1], 0x28
	s_load_dwordx2 s[26:27], s[0:1], 0x40
	s_load_dwordx2 s[28:29], s[0:1], 0x48
	s_and_b32 s12, s2, 7
	s_lshr_b32 s13, s2, 3
	s_lshl_b32 s12, s12, 5
	s_add_u32 s12, s12, s13
	s_and_b32 s13, s12, 3
	s_lshl_b32 s30, s13, 2
	s_lshr_b32 s12, s12, 2
	s_lshl_b32 s12, s12, 7
	s_mul_i32 s13, s13, 0xc0
	v_lshrrev_b32_e32 v1, 6, v0
	v_and_b32_e32 v14, 7, v0
	v_bfe_u32 v15, v0, 4, 3
	v_xor_b32_e32 v14, v14, v15
	v_readfirstlane_b32 s14, v1
	v_lshrrev_b32_e32 v15, 3, v0
	v_mul_u32_u24_e32 v15, 0x600, v15
	v_lshl_add_u32 v2, v14, 4, v15
	s_mov_b32 s22, 0xc000
	v_add_u32_e32 v3, s22, v2
	v_add_u32_e32 v4, s22, v3
	v_add_u32_e32 v5, s22, v4
	v_add_u32_e32 v6, s22, v5
	v_add_u32_e32 v7, s22, v6
	v_and_b32_e32 v14, 15, v0
	v_bfe_u32 v15, v0, 4, 2
	v_lshrrev_b32_e32 v16, 1, v14
	v_xor_b32_e32 v16, v16, v15
	v_lshlrev_b32_e32 v16, 4, v16
	v_bfe_u32 v17, v0, 7, 1
	v_bfe_u32 v18, v0, 6, 1
	v_lshl_add_u32 v19, v17, 6, v14
	v_lshl_add_u32 v8, v19, 7, v16
	v_mul_u32_u24_e32 v19, 0x60, v18
	v_add_u32_e32 v19, v19, v14
	v_lshl_add_u32 v9, v19, 7, v16
	v_add_u32_e32 v9, 0x4000, v9
	v_lshl_add_u32 v19, v17, 6, v14
	v_add_u32_e32 v19, s12, v19
	v_mul_u32_u24_e32 v19, 0xc00, v19
	v_mul_u32_u24_e32 v60, 0x60, v18
	v_lshl_add_u32 v60, v15, 2, v60
	v_add_u32_e32 v60, s13, v60
	v_lshl_add_u32 v56, v60, 2, v19
	s_mov_b32 s22, 0xc000
	v_add_u32_e32 v57, s22, v56
	v_add_u32_e32 v58, s22, v57
	v_add_u32_e32 v59, s22, v58
	v_mul_u32_u24_e32 v61, 0x60, v18
	v_lshl_add_u32 v61, v15, 2, v61
	v_add_u32_e32 v61, s13, v61
	v_lshlrev_b32_e32 v60, 2, v61
	s_waitcnt lgkmcnt(0)
	s_mul_i32 s22, s12, 0x600
	s_add_u32 s16, s4, s22
	s_addc_u32 s17, s5, 0
	s_mul_i32 s22, s13, 0x600
	s_add_u32 s18, s6, s22
	s_addc_u32 s19, s7, 0
	s_lshl_b32 s20, s14, 10
	s_mov_b32 s21, 0
	s_add_u32 m0, s20, 0x0
	s_nop 0
	global_load_lds_dwordx4 v2, s[16:17]
	s_add_u32 m0, s20, 0x1000
	s_nop 0
	global_load_lds_dwordx4 v3, s[16:17]
	s_add_u32 m0, s20, 0x2000
	s_nop 0
	global_load_lds_dwordx4 v4, s[16:17]
	s_add_u32 m0, s20, 0x3000
	s_nop 0
	global_load_lds_dwordx4 v5, s[16:17]
	s_add_u32 m0, s20, 0x4000
	s_nop 0
	global_load_lds_dwordx4 v2, s[18:19]
	s_add_u32 m0, s20, 0x5000
	s_nop 0
	global_load_lds_dwordx4 v3, s[18:19]
	s_add_u32 m0, s20, 0x6000
	s_nop 0
	global_load_lds_dwordx4 v4, s[18:19]
	s_add_u32 m0, s20, 0x7000
	s_nop 0
	global_load_lds_dwordx4 v5, s[18:19]
	s_add_u32 m0, s20, 0x8000
	s_nop 0
	global_load_lds_dwordx4 v6, s[18:19]
	s_add_u32 m0, s20, 0x9000
	s_nop 0
	global_load_lds_dwordx4 v7, s[18:19]
	s_add_u32 s16, s16, 0x80
	s_addc_u32 s17, s17, 0
	s_add_u32 s18, s18, 0x80
	s_addc_u32 s19, s19, 0
	s_add_u32 s20, s20, 0xa000
	s_sub_u32 s22, s20, 0x28000
	s_cmp_ge_u32 s20, 0x28000
	s_cselect_b32 s20, s22, s20
	s_add_u32 m0, s20, 0x0
	s_nop 0
	global_load_lds_dwordx4 v2, s[16:17]
	s_add_u32 m0, s20, 0x1000
	s_nop 0
	global_load_lds_dwordx4 v3, s[16:17]
	s_add_u32 m0, s20, 0x2000
	s_nop 0
	global_load_lds_dwordx4 v4, s[16:17]
	s_add_u32 m0, s20, 0x3000
	s_nop 0
	global_load_lds_dwordx4 v5, s[16:17]
	s_add_u32 m0, s20, 0x4000
	s_nop 0
	global_load_lds_dwordx4 v2, s[18:19]
	s_add_u32 m0, s20, 0x5000
	s_nop 0
	global_load_lds_dwordx4 v3, s[18:19]
	s_add_u32 m0, s20, 0x6000
	s_nop 0
	global_load_lds_dwordx4 v4, s[18:19]
	s_add_u32 m0, s20, 0x7000
	s_nop 0
	global_load_lds_dwordx4 v5, s[18:19]
	s_add_u32 m0, s20, 0x8000
	s_nop 0
	global_load_lds_dwordx4 v6, s[18:19]
	s_add_u32 m0, s20, 0x9000
	s_nop 0
	global_load_lds_dwordx4 v7, s[18:19]
	s_add_u32 s16, s16, 0x80
	s_addc_u32 s17, s17, 0
	s_add_u32 s18, s18, 0x80
	s_addc_u32 s19, s19, 0
	s_add_u32 s20, s20, 0xa000
	s_sub_u32 s22, s20, 0x28000
	s_cmp_ge_u32 s20, 0x28000
	s_cselect_b32 s20, s22, s20
	s_add_u32 m0, s20, 0x0
	s_nop 0
	global_load_lds_dwordx4 v2, s[16:17]
	s_add_u32 m0, s20, 0x1000
	s_nop 0
	global_load_lds_dwordx4 v3, s[16:17]
	s_add_u32 m0, s20, 0x2000
	s_nop 0
	global_load_lds_dwordx4 v4, s[16:17]
	s_add_u32 m0, s20, 0x3000
	s_nop 0
	global_load_lds_dwordx4 v5, s[16:17]
	s_add_u32 m0, s20, 0x4000
	s_nop 0
	global_load_lds_dwordx4 v2, s[18:19]
	s_add_u32 m0, s20, 0x5000
	s_nop 0
	global_load_lds_dwordx4 v3, s[18:19]
	s_add_u32 m0, s20, 0x6000
	s_nop 0
	global_load_lds_dwordx4 v4, s[18:19]
	s_add_u32 m0, s20, 0x7000
	s_nop 0
	global_load_lds_dwordx4 v5, s[18:19]
	s_add_u32 m0, s20, 0x8000
	s_nop 0
	global_load_lds_dwordx4 v6, s[18:19]
	s_add_u32 m0, s20, 0x9000
	s_nop 0
	global_load_lds_dwordx4 v7, s[18:19]
	s_add_u32 s16, s16, 0x80
	s_addc_u32 s17, s17, 0
	s_add_u32 s18, s18, 0x80
	s_addc_u32 s19, s19, 0
	s_add_u32 s20, s20, 0xa000
	s_sub_u32 s22, s20, 0x28000
	s_cmp_ge_u32 s20, 0x28000
	s_cselect_b32 s20, s22, s20
	s_add_u32 m0, s20, 0x0
	s_nop 0
	global_load_lds_dwordx4 v2, s[16:17]
	s_add_u32 m0, s20, 0x1000
	s_nop 0
	global_load_lds_dwordx4 v3, s[16:17]
	s_add_u32 m0, s20, 0x2000
	s_nop 0
	global_load_lds_dwordx4 v4, s[16:17]
	s_add_u32 m0, s20, 0x3000
	s_nop 0
	global_load_lds_dwordx4 v5, s[16:17]
	s_add_u32 m0, s20, 0x4000
	s_nop 0
	global_load_lds_dwordx4 v2, s[18:19]
	v_mov_b32_e32 v64, 0
	v_mov_b32_e32 v65, 0
	v_mov_b32_e32 v66, 0
	v_mov_b32_e32 v67, 0
	v_mov_b32_e32 v68, 0
	v_mov_b32_e32 v69, 0
	v_mov_b32_e32 v70, 0
	v_mov_b32_e32 v71, 0
	v_mov_b32_e32 v72, 0
	v_mov_b32_e32 v73, 0
	v_mov_b32_e32 v74, 0
	v_mov_b32_e32 v75, 0
	v_mov_b32_e32 v76, 0
	v_mov_b32_e32 v77, 0
	v_mov_b32_e32 v78, 0
	v_mov_b32_e32 v79, 0
	v_mov_b32_e32 v80, 0
	v_mov_b32_e32 v81, 0
	v_mov_b32_e32 v82, 0
	v_mov_b32_e32 v83, 0
	v_mov_b32_e32 v84, 0
	v_mov_b32_e32 v85, 0
	v_mov_b32_e32 v86, 0
	v_mov_b32_e32 v87, 0
	v_mov_b32_e32 v88, 0
	v_mov_b32_e32 v89, 0
	v_mov_b32_e32 v90, 0
	v_mov_b32_e32 v91, 0
	v_mov_b32_e32 v92, 0
	v_mov_b32_e32 v93, 0
	v_mov_b32_e32 v94, 0
	v_mov_b32_e32 v95, 0
	v_mov_b32_e32 v96, 0
	v_mov_b32_e32 v97, 0
	v_mov_b32_e32 v98, 0
	v_mov_b32_e32 v99, 0
	v_mov_b32_e32 v100, 0
	v_mov_b32_e32 v101, 0
	v_mov_b32_e32 v102, 0
	v_mov_b32_e32 v103, 0
	v_mov_b32_e32 v104, 0
	v_mov_b32_e32 v105, 0
	v_mov_b32_e32 v106, 0
	v_mov_b32_e32 v107, 0
	v_mov_b32_e32 v108, 0
	v_mov_b32_e32 v109, 0
	v_mov_b32_e32 v110, 0
	v_mov_b32_e32 v111, 0
	v_mov_b32_e32 v112, 0
	v_mov_b32_e32 v113, 0
	v_mov_b32_e32 v114, 0
	v_mov_b32_e32 v115, 0
	v_mov_b32_e32 v116, 0
	v_mov_b32_e32 v117, 0
	v_mov_b32_e32 v118, 0
	v_mov_b32_e32 v119, 0
	v_mov_b32_e32 v120, 0
	v_mov_b32_e32 v121, 0
	v_mov_b32_e32 v122, 0
	v_mov_b32_e32 v123, 0
	v_mov_b32_e32 v124, 0
	v_mov_b32_e32 v125, 0
	v_mov_b32_e32 v126, 0
	v_mov_b32_e32 v127, 0
	v_mov_b32_e32 v128, 0
	v_mov_b32_e32 v129, 0
	v_mov_b32_e32 v130, 0
	v_mov_b32_e32 v131, 0
	v_mov_b32_e32 v132, 0
	v_mov_b32_e32 v133, 0
	v_mov_b32_e32 v134, 0
	v_mov_b32_e32 v135, 0
	v_mov_b32_e32 v136, 0
	v_mov_b32_e32 v137, 0
	v_mov_b32_e32 v138, 0
	v_mov_b32_e32 v139, 0
	v_mov_b32_e32 v140, 0
	v_mov_b32_e32 v141, 0
	v_mov_b32_e32 v142, 0
	v_mov_b32_e32 v143, 0
	v_mov_b32_e32 v144, 0
	v_mov_b32_e32 v145, 0
	v_mov_b32_e32 v146, 0
	v_mov_b32_e32 v147, 0
	v_mov_b32_e32 v148, 0
	v_mov_b32_e32 v149, 0
	v_mov_b32_e32 v150, 0
	v_mov_b32_e32 v151, 0
	v_mov_b32_e32 v152, 0
	v_mov_b32_e32 v153, 0
	v_mov_b32_e32 v154, 0
	v_mov_b32_e32 v155, 0
	v_mov_b32_e32 v156, 0
	v_mov_b32_e32 v157, 0
	v_mov_b32_e32 v158, 0
	v_mov_b32_e32 v159, 0
	s_waitcnt vmcnt(25)
	s_barrier
	v_add_u32_e32 v10, s21, v8
	v_add_u32_e32 v12, s21, v9
	v_xor_b32_e32 v11, 64, v10
	v_xor_b32_e32 v13, 64, v12
	s_add_u32 s21, s21, 0xa000
	s_sub_u32 s23, s21, 0x28000
	s_cmp_ge_u32 s21, 0x28000
	s_cselect_b32 s21, s23, s21
	ds_read_b128 v[160:163], v10 offset:0
	ds_read_b128 v[164:167], v10 offset:2048
	ds_read_b128 v[168:171], v10 offset:4096
	ds_read_b128 v[172:175], v10 offset:6144
	ds_read_b128 v[176:179], v12 offset:0
	ds_read_b128 v[180:183], v12 offset:2048
	ds_read_b128 v[184:187], v12 offset:4096
	ds_read_b128 v[188:191], v12 offset:6144
	ds_read_b128 v[192:195], v12 offset:8192
	ds_read_b128 v[196:199], v12 offset:10240
	s_mov_b32 s15, 0

_Z7gemm128ILi2ELi128EEv8GemmArgs:
	s_cmp_lt_u32 s2, 0x100
	s_cbranch_scc1 .Lup_body
	s_endpgm
.Lup_body:
	s_load_dwordx4 s[4:7], s[0:1], 0x0
	s_load_dwordx2 s[8:9], s[0:1], 0x20
	s_load_dwordx2 s[10:11], s[0:1], 0x48
	s_and_b32 s12, s2, 7
	s_lshr_b32 s13, s2, 3
	s_lshl_b32 s12, s12, 5
	s_add_u32 s12, s12, s13
	s_and_b32 s13, s12, 3
	s_lshr_b32 s12, s12, 2
	s_lshl_b32 s12, s12, 7
	s_lshl_b32 s13, s13, 8
	s_add_u32 s13, s13, 0x800
	s_mov_b32 s24, 0xc0135761
	s_mov_b32 s26, 0x3dd2d3e8
	s_mov_b32 s27, 0x3dd2d3e8
	s_mov_b32 s28, 0xc0135761
	s_mov_b32 s29, 0xc0135761
	s_mov_b32 s30, 1.0
	s_mov_b32 s31, 1.0
	v_lshrrev_b32_e32 v1, 6, v0
	v_and_b32_e32 v24, 7, v0
	v_bfe_u32 v25, v0, 4, 3
	v_xor_b32_e32 v24, v24, v25
	v_readfirstlane_b32 s14, v1
	v_lshrrev_b32_e32 v25, 3, v0
	v_mul_u32_u24_e32 v25, 0x600, v25
	v_lshl_add_u32 v2, v24, 4, v25
	s_mov_b32 s22, 0xc000
	v_add_u32_e32 v3, s22, v2
	v_add_u32_e32 v4, s22, v3
	v_add_u32_e32 v5, s22, v4
	v_add_u32_e32 v6, s22, v5
	v_add_u32_e32 v7, s22, v6
	v_add_u32_e32 v8, s22, v7
	v_add_u32_e32 v9, s22, v8
	v_and_b32_e32 v24, 15, v0
	v_bfe_u32 v25, v0, 4, 2
	v_lshrrev_b32_e32 v26, 1, v24
	v_xor_b32_e32 v26, v26, v25
	v_lshlrev_b32_e32 v26, 4, v26
	v_bfe_u32 v27, v0, 7, 1
	v_bfe_u32 v28, v0, 6, 1
	v_lshl_add_u32 v29, v27, 6, v24
	v_lshl_add_u32 v10, v29, 7, v26
	v_lshl_add_u32 v30, v28, 7, v24
	v_lshl_add_u32 v11, v30, 7, v26
	v_add_u32_e32 v11, 0x4000, v11
	v_add_u32_e32 v29, s12, v29
	v_lshlrev_b32_e32 v21, 6, v29
	v_mul_u32_u24_e32 v29, 0x1800, v29
	v_lshlrev_b32_e32 v30, 7, v28
	v_lshl_add_u32 v30, v25, 2, v30
	v_add_u32_e32 v30, s13, v30
	v_lshl_add_u32 v16, v30, 1, v29
	s_mov_b32 s22, 0x18000
	v_add_u32_e32 v17, s22, v16
	v_add_u32_e32 v18, s22, v17
	v_add_u32_e32 v19, s22, v18
	s_waitcnt lgkmcnt(0)
	s_mul_i32 s22, s12, 0x600
	s_add_u32 s16, s4, s22
	s_addc_u32 s17, s5, 0
	s_mul_i32 s22, s13, 0x600
	s_add_u32 s18, s6, s22
	s_addc_u32 s19, s7, 0
	s_lshl_b32 s20, s14, 10
	s_mov_b32 s21, 0
	s_add_u32 m0, s20, 0x0
	s_nop 0
	global_load_lds_dwordx4 v2, s[16:17]
	s_add_u32 m0, s20, 0x1000
	s_nop 0
	global_load_lds_dwordx4 v3, s[16:17]
	s_add_u32 m0, s20, 0x2000
	s_nop 0
	global_load_lds_dwordx4 v4, s[16:17]
	s_add_u32 m0, s20, 0x3000
	s_nop 0
	global_load_lds_dwordx4 v5, s[16:17]
	s_add_u32 m0, s20, 0x4000
	s_nop 0
	global_load_lds_dwordx4 v2, s[18:19]
	s_add_u32 m0, s20, 0x5000
	s_nop 0
	global_load_lds_dwordx4 v3, s[18:19]
	s_add_u32 m0, s20, 0x6000
	s_nop 0
	global_load_lds_dwordx4 v4, s[18:19]
	s_add_u32 m0, s20, 0x7000
	s_nop 0
	global_load_lds_dwordx4 v5, s[18:19]
	s_add_u32 m0, s20, 0x8000
	s_nop 0
	global_load_lds_dwordx4 v6, s[18:19]
	s_add_u32 m0, s20, 0x9000
	s_nop 0
	global_load_lds_dwordx4 v7, s[18:19]
	s_add_u32 m0, s20, 0xa000
	s_nop 0
	global_load_lds_dwordx4 v8, s[18:19]
	s_add_u32 m0, s20, 0xb000
	s_nop 0
	global_load_lds_dwordx4 v9, s[18:19]
	s_add_u32 s16, s16, 0x80
	s_addc_u32 s17, s17, 0
	s_add_u32 s18, s18, 0x80
	s_addc_u32 s19, s19, 0
	s_add_u32 s20, s20, 0xc000
	s_sub_u32 s22, s20, 0x24000
	s_cmp_ge_u32 s20, 0x24000
	s_cselect_b32 s20, s22, s20
	s_add_u32 m0, s20, 0x0
	s_nop 0
	global_load_lds_dwordx4 v2, s[16:17]
	s_add_u32 m0, s20, 0x1000
	s_nop 0
	global_load_lds_dwordx4 v3, s[16:17]
	s_add_u32 m0, s20, 0x2000
	s_nop 0
	global_load_lds_dwordx4 v4, s[16:17]
	s_add_u32 m0, s20, 0x3000
	s_nop 0
	global_load_lds_dwordx4 v5, s[16:17]
	s_add_u32 m0, s20, 0x4000
	s_nop 0
	global_load_lds_dwordx4 v2, s[18:19]
	s_add_u32 m0, s20, 0x5000
	s_nop 0
	global_load_lds_dwordx4 v3, s[18:19]
	s_add_u32 m0, s20, 0x6000
	s_nop 0
	global_load_lds_dwordx4 v4, s[18:19]
	s_add_u32 m0, s20, 0x7000
	s_nop 0
	global_load_lds_dwordx4 v5, s[18:19]
	s_add_u32 m0, s20, 0x8000
	s_nop 0
	global_load_lds_dwordx4 v6, s[18:19]
	s_add_u32 m0, s20, 0x9000
	s_nop 0
	global_load_lds_dwordx4 v7, s[18:19]
	s_add_u32 m0, s20, 0xa000
	s_nop 0
	global_load_lds_dwordx4 v8, s[18:19]
	s_add_u32 m0, s20, 0xb000
	s_nop 0
	global_load_lds_dwordx4 v9, s[18:19]
	s_add_u32 s16, s16, 0x80
	s_addc_u32 s17, s17, 0
	s_add_u32 s18, s18, 0x80
	s_addc_u32 s19, s19, 0
	s_add_u32 s20, s20, 0xc000
	s_sub_u32 s22, s20, 0x24000
	s_cmp_ge_u32 s20, 0x24000
	s_cselect_b32 s20, s22, s20
	s_add_u32 m0, s20, 0x0
	s_nop 0
	global_load_lds_dwordx4 v2, s[16:17]
	s_add_u32 m0, s20, 0x1000
	s_nop 0
	global_load_lds_dwordx4 v3, s[16:17]
	s_add_u32 m0, s20, 0x2000
	s_nop 0
	global_load_lds_dwordx4 v4, s[16:17]
	s_add_u32 m0, s20, 0x3000
	s_nop 0
	global_load_lds_dwordx4 v5, s[16:17]
	s_add_u32 m0, s20, 0x4000
	s_nop 0
	global_load_lds_dwordx4 v2, s[18:19]
	s_add_u32 m0, s20, 0x5000
	s_nop 0
	global_load_lds_dwordx4 v3, s[18:19]
	v_mov_b32_e32 v128, 0
	v_mov_b32_e32 v129, 0
	v_mov_b32_e32 v130, 0
	v_mov_b32_e32 v131, 0
	v_mov_b32_e32 v132, 0
	v_mov_b32_e32 v133, 0
	v_mov_b32_e32 v134, 0
	v_mov_b32_e32 v135, 0
	v_mov_b32_e32 v136, 0
	v_mov_b32_e32 v137, 0
	v_mov_b32_e32 v138, 0
	v_mov_b32_e32 v139, 0
	v_mov_b32_e32 v140, 0
	v_mov_b32_e32 v141, 0
	v_mov_b32_e32 v142, 0
	v_mov_b32_e32 v143, 0
	v_mov_b32_e32 v144, 0
	v_mov_b32_e32 v145, 0
	v_mov_b32_e32 v146, 0
	v_mov_b32_e32 v147, 0
	v_mov_b32_e32 v148, 0
	v_mov_b32_e32 v149, 0
	v_mov_b32_e32 v150, 0
	v_mov_b32_e32 v151, 0
	v_mov_b32_e32 v152, 0
	v_mov_b32_e32 v153, 0
	v_mov_b32_e32 v154, 0
	v_mov_b32_e32 v155, 0
	v_mov_b32_e32 v156, 0
	v_mov_b32_e32 v157, 0
	v_mov_b32_e32 v158, 0
	v_mov_b32_e32 v159, 0
	v_mov_b32_e32 v160, 0
	v_mov_b32_e32 v161, 0
	v_mov_b32_e32 v162, 0
	v_mov_b32_e32 v163, 0
	v_mov_b32_e32 v164, 0
	v_mov_b32_e32 v165, 0
	v_mov_b32_e32 v166, 0
	v_mov_b32_e32 v167, 0
	v_mov_b32_e32 v168, 0
	v_mov_b32_e32 v169, 0
	v_mov_b32_e32 v170, 0
	v_mov_b32_e32 v171, 0
	v_mov_b32_e32 v172, 0
	v_mov_b32_e32 v173, 0
	v_mov_b32_e32 v174, 0
	v_mov_b32_e32 v175, 0
	v_mov_b32_e32 v176, 0
	v_mov_b32_e32 v177, 0
	v_mov_b32_e32 v178, 0
	v_mov_b32_e32 v179, 0
	v_mov_b32_e32 v180, 0
	v_mov_b32_e32 v181, 0
	v_mov_b32_e32 v182, 0
	v_mov_b32_e32 v183, 0
	v_mov_b32_e32 v184, 0
	v_mov_b32_e32 v185, 0
	v_mov_b32_e32 v186, 0
	v_mov_b32_e32 v187, 0
	v_mov_b32_e32 v188, 0
	v_mov_b32_e32 v189, 0
	v_mov_b32_e32 v190, 0
	v_mov_b32_e32 v191, 0
	v_mov_b32_e32 v192, 0
	v_mov_b32_e32 v193, 0
	v_mov_b32_e32 v194, 0
	v_mov_b32_e32 v195, 0
	v_mov_b32_e32 v196, 0
	v_mov_b32_e32 v197, 0
	v_mov_b32_e32 v198, 0
	v_mov_b32_e32 v199, 0
	v_mov_b32_e32 v200, 0
	v_mov_b32_e32 v201, 0
	v_mov_b32_e32 v202, 0
	v_mov_b32_e32 v203, 0
	v_mov_b32_e32 v204, 0
	v_mov_b32_e32 v205, 0
	v_mov_b32_e32 v206, 0
	v_mov_b32_e32 v207, 0
	v_mov_b32_e32 v208, 0
	v_mov_b32_e32 v209, 0
	v_mov_b32_e32 v210, 0
	v_mov_b32_e32 v211, 0
	v_mov_b32_e32 v212, 0
	v_mov_b32_e32 v213, 0
	v_mov_b32_e32 v214, 0
	v_mov_b32_e32 v215, 0
	v_mov_b32_e32 v216, 0
	v_mov_b32_e32 v217, 0
	v_mov_b32_e32 v218, 0
	v_mov_b32_e32 v219, 0
	v_mov_b32_e32 v220, 0
	v_mov_b32_e32 v221, 0
	v_mov_b32_e32 v222, 0
	v_mov_b32_e32 v223, 0
	v_mov_b32_e32 v224, 0
	v_mov_b32_e32 v225, 0
	v_mov_b32_e32 v226, 0
	v_mov_b32_e32 v227, 0
	v_mov_b32_e32 v228, 0
	v_mov_b32_e32 v229, 0
	v_mov_b32_e32 v230, 0
	v_mov_b32_e32 v231, 0
	v_mov_b32_e32 v232, 0
	v_mov_b32_e32 v233, 0
	v_mov_b32_e32 v234, 0
	v_mov_b32_e32 v235, 0
	v_mov_b32_e32 v236, 0
	v_mov_b32_e32 v237, 0
	v_mov_b32_e32 v238, 0
	v_mov_b32_e32 v239, 0
	v_mov_b32_e32 v240, 0
	v_mov_b32_e32 v241, 0
	v_mov_b32_e32 v242, 0
	v_mov_b32_e32 v243, 0
	v_mov_b32_e32 v244, 0
	v_mov_b32_e32 v245, 0
	v_mov_b32_e32 v246, 0
	v_mov_b32_e32 v247, 0
	v_mov_b32_e32 v248, 0
	v_mov_b32_e32 v249, 0
	v_mov_b32_e32 v250, 0
	v_mov_b32_e32 v251, 0
	v_mov_b32_e32 v252, 0
	v_mov_b32_e32 v253, 0
	v_mov_b32_e32 v254, 0
	v_mov_b32_e32 v255, 0
	s_waitcnt vmcnt(18)
	s_barrier
	v_add_u32_e32 v12, s21, v10
	v_add_u32_e32 v14, s21, v11
	v_xor_b32_e32 v13, 64, v12
	v_xor_b32_e32 v15, 64, v14
	s_add_u32 s21, s21, 0xc000
	s_sub_u32 s23, s21, 0x24000
	s_cmp_ge_u32 s21, 0x24000
	s_cselect_b32 s21, s23, s21
	ds_read_b128 v[32:35], v12 offset:0
	ds_read_b128 v[36:39], v12 offset:2048
	ds_read_b128 v[40:43], v12 offset:4096
	ds_read_b128 v[44:47], v12 offset:6144
	ds_read_b128 v[48:51], v14 offset:0
	ds_read_b128 v[52:55], v14 offset:2048
	ds_read_b128 v[56:59], v14 offset:4096
	ds_read_b128 v[60:63], v14 offset:6144
	ds_read_b128 v[64:67], v14 offset:8192
	ds_read_b128 v[68:71], v14 offset:10240
	ds_read_b128 v[72:75], v14 offset:12288
	ds_read_b128 v[76:79], v14 offset:14336
	s_mov_b32 s15, 0

_Z7gemm128ILi3ELi96EEv8GemmArgs:
	s_cmp_lt_u32 s2, 0x100
	s_cbranch_scc1 .Ldn_body
	s_endpgm
.Ldn_body:
	s_load_dwordx4 s[4:7], s[0:1], 0x0
	s_load_dwordx2 s[8:9], s[0:1], 0x20
	s_load_dwordx2 s[10:11], s[0:1], 0x38
	s_and_b32 s12, s2, 7
	s_lshr_b32 s13, s2, 3
	s_lshl_b32 s12, s12, 5
	s_add_u32 s12, s12, s13
	s_and_b32 s13, s12, 3
	s_lshr_b32 s12, s12, 2
	s_lshl_b32 s12, s12, 7
	s_mul_i32 s13, s13, 0xc0
	v_lshrrev_b32_e32 v1, 6, v0
	v_and_b32_e32 v14, 7, v0
	v_bfe_u32 v15, v0, 4, 3
	v_xor_b32_e32 v14, v14, v15
	v_readfirstlane_b32 s14, v1
	v_lshrrev_b32_e32 v15, 3, v0
	v_mul_u32_u24_e32 v15, 0x1800, v15
	v_lshl_add_u32 v2, v14, 4, v15
	s_mov_b32 s22, 0x30000
	v_add_u32_e32 v3, s22, v2
	v_add_u32_e32 v4, s22, v3
	v_add_u32_e32 v5, s22, v4
	v_add_u32_e32 v6, s22, v5
	v_add_u32_e32 v7, s22, v6
	v_and_b32_e32 v14, 15, v0
	v_bfe_u32 v15, v0, 4, 2
	v_lshrrev_b32_e32 v16, 1, v14
	v_xor_b32_e32 v16, v16, v15
	v_lshlrev_b32_e32 v16, 4, v16
	v_bfe_u32 v17, v0, 7, 1
	v_bfe_u32 v18, v0, 6, 1
	v_lshl_add_u32 v19, v17, 6, v14
	v_lshl_add_u32 v8, v19, 7, v16
	v_mul_u32_u24_e32 v19, 0x60, v18
	v_add_u32_e32 v19, v19, v14
	v_lshl_add_u32 v9, v19, 7, v16
	v_add_u32_e32 v9, 0x4000, v9
	v_lshl_add_u32 v19, v17, 6, v14
	v_add_u32_e32 v19, s12, v19
	v_mul_u32_u24_e32 v19, 0xc00, v19
	v_mul_u32_u24_e32 v60, 0x60, v18
	v_lshl_add_u32 v60, v15, 2, v60
	v_add_u32_e32 v60, s13, v60
	v_lshl_add_u32 v56, v60, 2, v19
	s_mov_b32 s22, 0xc000
	v_add_u32_e32 v57, s22, v56
	v_add_u32_e32 v58, s22, v57
	v_add_u32_e32 v59, s22, v58
	s_waitcnt lgkmcnt(0)
	s_mul_i32 s22, s12, 0x1800
	s_add_u32 s16, s4, s22
	s_addc_u32 s17, s5, 0
	s_mul_i32 s22, s13, 0x1800
	s_add_u32 s18, s6, s22
	s_addc_u32 s19, s7, 0
	s_lshl_b32 s20, s14, 10
	s_mov_b32 s21, 0
	s_add_u32 m0, s20, 0x0
	s_nop 0
	global_load_lds_dwordx4 v2, s[16:17]
	s_add_u32 m0, s20, 0x1000
	s_nop 0
	global_load_lds_dwordx4 v3, s[16:17]
	s_add_u32 m0, s20, 0x2000
	s_nop 0
	global_load_lds_dwordx4 v4, s[16:17]
	s_add_u32 m0, s20, 0x3000
	s_nop 0
	global_load_lds_dwordx4 v5, s[16:17]
	s_add_u32 m0, s20, 0x4000
	s_nop 0
	global_load_lds_dwordx4 v2, s[18:19]
	s_add_u32 m0, s20, 0x5000
	s_nop 0
	global_load_lds_dwordx4 v3, s[18:19]
	s_add_u32 m0, s20, 0x6000
	s_nop 0
	global_load_lds_dwordx4 v4, s[18:19]
	s_add_u32 m0, s20, 0x7000
	s_nop 0
	global_load_lds_dwordx4 v5, s[18:19]
	s_add_u32 m0, s20, 0x8000
	s_nop 0
	global_load_lds_dwordx4 v6, s[18:19]
	s_add_u32 m0, s20, 0x9000
	s_nop 0
	global_load_lds_dwordx4 v7, s[18:19]
	s_add_u32 s16, s16, 0x80
	s_addc_u32 s17, s17, 0
	s_add_u32 s18, s18, 0x80
	s_addc_u32 s19, s19, 0
	s_add_u32 s20, s20, 0xa000
	s_sub_u32 s22, s20, 0x28000
	s_cmp_ge_u32 s20, 0x28000
	s_cselect_b32 s20, s22, s20
	s_add_u32 m0, s20, 0x0
	s_nop 0
	global_load_lds_dwordx4 v2, s[16:17]
	s_add_u32 m0, s20, 0x1000
	s_nop 0
	global_load_lds_dwordx4 v3, s[16:17]
	s_add_u32 m0, s20, 0x2000
	s_nop 0
	global_load_lds_dwordx4 v4, s[16:17]
	s_add_u32 m0, s20, 0x3000
	s_nop 0
	global_load_lds_dwordx4 v5, s[16:17]
	s_add_u32 m0, s20, 0x4000
	s_nop 0
	global_load_lds_dwordx4 v2, s[18:19]
	s_add_u32 m0, s20, 0x5000
	s_nop 0
	global_load_lds_dwordx4 v3, s[18:19]
	s_add_u32 m0, s20, 0x6000
	s_nop 0
	global_load_lds_dwordx4 v4, s[18:19]
	s_add_u32 m0, s20, 0x7000
	s_nop 0
	global_load_lds_dwordx4 v5, s[18:19]
	s_add_u32 m0, s20, 0x8000
	s_nop 0
	global_load_lds_dwordx4 v6, s[18:19]
	s_add_u32 m0, s20, 0x9000
	s_nop 0
	global_load_lds_dwordx4 v7, s[18:19]
	s_add_u32 s16, s16, 0x80
	s_addc_u32 s17, s17, 0
	s_add_u32 s18, s18, 0x80
	s_addc_u32 s19, s19, 0
	s_add_u32 s20, s20, 0xa000
	s_sub_u32 s22, s20, 0x28000
	s_cmp_ge_u32 s20, 0x28000
	s_cselect_b32 s20, s22, s20
	s_add_u32 m0, s20, 0x0
	s_nop 0
	global_load_lds_dwordx4 v2, s[16:17]
	s_add_u32 m0, s20, 0x1000
	s_nop 0
	global_load_lds_dwordx4 v3, s[16:17]
	s_add_u32 m0, s20, 0x2000
	s_nop 0
	global_load_lds_dwordx4 v4, s[16:17]
	s_add_u32 m0, s20, 0x3000
	s_nop 0
	global_load_lds_dwordx4 v5, s[16:17]
	s_add_u32 m0, s20, 0x4000
	s_nop 0
	global_load_lds_dwordx4 v2, s[18:19]
	s_add_u32 m0, s20, 0x5000
	s_nop 0
	global_load_lds_dwordx4 v3, s[18:19]
	s_add_u32 m0, s20, 0x6000
	s_nop 0
	global_load_lds_dwordx4 v4, s[18:19]
	s_add_u32 m0, s20, 0x7000
	s_nop 0
	global_load_lds_dwordx4 v5, s[18:19]
	s_add_u32 m0, s20, 0x8000
	s_nop 0
	global_load_lds_dwordx4 v6, s[18:19]
	s_add_u32 m0, s20, 0x9000
	s_nop 0
	global_load_lds_dwordx4 v7, s[18:19]
	s_add_u32 s16, s16, 0x80
	s_addc_u32 s17, s17, 0
	s_add_u32 s18, s18, 0x80
	s_addc_u32 s19, s19, 0
	s_add_u32 s20, s20, 0xa000
	s_sub_u32 s22, s20, 0x28000
	s_cmp_ge_u32 s20, 0x28000
	s_cselect_b32 s20, s22, s20
	s_add_u32 m0, s20, 0x0
	s_nop 0
	global_load_lds_dwordx4 v2, s[16:17]
	s_add_u32 m0, s20, 0x1000
	s_nop 0
	global_load_lds_dwordx4 v3, s[16:17]
	s_add_u32 m0, s20, 0x2000
	s_nop 0
	global_load_lds_dwordx4 v4, s[16:17]
	s_add_u32 m0, s20, 0x3000
	s_nop 0
	global_load_lds_dwordx4 v5, s[16:17]
	s_add_u32 m0, s20, 0x4000
	s_nop 0
	global_load_lds_dwordx4 v2, s[18:19]
	v_mov_b32_e32 v64, 0
	v_mov_b32_e32 v65, 0
	v_mov_b32_e32 v66, 0
	v_mov_b32_e32 v67, 0
	v_mov_b32_e32 v68, 0
	v_mov_b32_e32 v69, 0
	v_mov_b32_e32 v70, 0
	v_mov_b32_e32 v71, 0
	v_mov_b32_e32 v72, 0
	v_mov_b32_e32 v73, 0
	v_mov_b32_e32 v74, 0
	v_mov_b32_e32 v75, 0
	v_mov_b32_e32 v76, 0
	v_mov_b32_e32 v77, 0
	v_mov_b32_e32 v78, 0
	v_mov_b32_e32 v79, 0
	v_mov_b32_e32 v80, 0
	v_mov_b32_e32 v81, 0
	v_mov_b32_e32 v82, 0
	v_mov_b32_e32 v83, 0
	v_mov_b32_e32 v84, 0
	v_mov_b32_e32 v85, 0
	v_mov_b32_e32 v86, 0
	v_mov_b32_e32 v87, 0
	v_mov_b32_e32 v88, 0
	v_mov_b32_e32 v89, 0
	v_mov_b32_e32 v90, 0
	v_mov_b32_e32 v91, 0
	v_mov_b32_e32 v92, 0
	v_mov_b32_e32 v93, 0
	v_mov_b32_e32 v94, 0
	v_mov_b32_e32 v95, 0
	v_mov_b32_e32 v96, 0
	v_mov_b32_e32 v97, 0
	v_mov_b32_e32 v98, 0
	v_mov_b32_e32 v99, 0
	v_mov_b32_e32 v100, 0
	v_mov_b32_e32 v101, 0
	v_mov_b32_e32 v102, 0
	v_mov_b32_e32 v103, 0
	v_mov_b32_e32 v104, 0
	v_mov_b32_e32 v105, 0
	v_mov_b32_e32 v106, 0
	v_mov_b32_e32 v107, 0
	v_mov_b32_e32 v108, 0
	v_mov_b32_e32 v109, 0
	v_mov_b32_e32 v110, 0
	v_mov_b32_e32 v111, 0
	v_mov_b32_e32 v112, 0
	v_mov_b32_e32 v113, 0
	v_mov_b32_e32 v114, 0
	v_mov_b32_e32 v115, 0
	v_mov_b32_e32 v116, 0
	v_mov_b32_e32 v117, 0
	v_mov_b32_e32 v118, 0
	v_mov_b32_e32 v119, 0
	v_mov_b32_e32 v120, 0
	v_mov_b32_e32 v121, 0
	v_mov_b32_e32 v122, 0
	v_mov_b32_e32 v123, 0
	v_mov_b32_e32 v124, 0
	v_mov_b32_e32 v125, 0
	v_mov_b32_e32 v126, 0
	v_mov_b32_e32 v127, 0
	v_mov_b32_e32 v128, 0
	v_mov_b32_e32 v129, 0
	v_mov_b32_e32 v130, 0
	v_mov_b32_e32 v131, 0
	v_mov_b32_e32 v132, 0
	v_mov_b32_e32 v133, 0
	v_mov_b32_e32 v134, 0
	v_mov_b32_e32 v135, 0
	v_mov_b32_e32 v136, 0
	v_mov_b32_e32 v137, 0
	v_mov_b32_e32 v138, 0
	v_mov_b32_e32 v139, 0
	v_mov_b32_e32 v140, 0
	v_mov_b32_e32 v141, 0
	v_mov_b32_e32 v142, 0
	v_mov_b32_e32 v143, 0
	v_mov_b32_e32 v144, 0
	v_mov_b32_e32 v145, 0
	v_mov_b32_e32 v146, 0
	v_mov_b32_e32 v147, 0
	v_mov_b32_e32 v148, 0
	v_mov_b32_e32 v149, 0
	v_mov_b32_e32 v150, 0
	v_mov_b32_e32 v151, 0
	v_mov_b32_e32 v152, 0
	v_mov_b32_e32 v153, 0
	v_mov_b32_e32 v154, 0
	v_mov_b32_e32 v155, 0
	v_mov_b32_e32 v156, 0
	v_mov_b32_e32 v157, 0
	v_mov_b32_e32 v158, 0
	v_mov_b32_e32 v159, 0
	s_waitcnt vmcnt(25)
	s_barrier
	v_add_u32_e32 v10, s21, v8
	v_add_u32_e32 v12, s21, v9
	v_xor_b32_e32 v11, 64, v10
	v_xor_b32_e32 v13, 64, v12
	s_add_u32 s21, s21, 0xa000
	s_sub_u32 s23, s21, 0x28000
	s_cmp_ge_u32 s21, 0x28000
	s_cselect_b32 s21, s23, s21
	ds_read_b128 v[160:163], v10 offset:0
	ds_read_b128 v[164:167], v10 offset:2048
	ds_read_b128 v[168:171], v10 offset:4096
	ds_read_b128 v[172:175], v10 offset:6144
	ds_read_b128 v[176:179], v12 offset:0
	ds_read_b128 v[180:183], v12 offset:2048
	ds_read_b128 v[184:187], v12 offset:4096
	ds_read_b128 v[188:191], v12 offset:6144
	ds_read_b128 v[192:195], v12 offset:8192
	ds_read_b128 v[196:199], v12 offset:10240
	s_mov_b32 s15, 0
.Ldn_loop:
	s_waitcnt lgkmcnt(0)
	v_mfma_f32_16x16x32_bf16 v[64:67], v[176:179], v[160:163], v[64:67]
	ds_read_b128 v[200:203], v11 offset:0
	v_mfma_f32_16x16x32_bf16 v[68:71], v[176:179], v[164:167], v[68:71]
	s_add_u32 m0, s20, 0x5000
	v_mfma_f32_16x16x32_bf16 v[72:75], v[176:179], v[168:171], v[72:75]
	ds_read_b128 v[204:207], v11 offset:2048
	v_mfma_f32_16x16x32_bf16 v[76:79], v[176:179], v[172:175], v[76:79]
	global_load_lds_dwordx4 v3, s[18:19]
	v_mfma_f32_16x16x32_bf16 v[80:83], v[180:183], v[160:163], v[80:83]
	ds_read_b128 v[208:211], v11 offset:4096
	v_mfma_f32_16x16x32_bf16 v[84:87], v[180:183], v[164:167], v[84:87]
	s_add_u32 m0, s20, 0x6000
	v_mfma_f32_16x16x32_bf16 v[88:91], v[180:183], v[168:171], v[88:91]
	ds_read_b128 v[212:215], v11 offset:6144
	v_mfma_f32_16x16x32_bf16 v[92:95], v[180:183], v[172:175], v[92:95]
	global_load_lds_dwordx4 v4, s[18:19]
	v_mfma_f32_16x16x32_bf16 v[96:99], v[184:187], v[160:163], v[96:99]
	ds_read_b128 v[216:219], v13 offset:0
	v_mfma_f32_16x16x32_bf16 v[100:103], v[184:187], v[164:167], v[100:103]
	s_add_u32 m0, s20, 0x7000
	v_mfma_f32_16x16x32_bf16 v[104:107], v[184:187], v[168:171], v[104:107]
	ds_read_b128 v[220:223], v13 offset:2048
	v_mfma_f32_16x16x32_bf16 v[108:111], v[184:187], v[172:175], v[108:111]
	global_load_lds_dwordx4 v5, s[18:19]
	v_mfma_f32_16x16x32_bf16 v[112:115], v[188:191], v[160:163], v[112:115]
	ds_read_b128 v[224:227], v13 offset:4096
	v_mfma_f32_16x16x32_bf16 v[116:119], v[188:191], v[164:167], v[116:119]
	s_add_u32 m0, s20, 0x8000
	v_mfma_f32_16x16x32_bf16 v[120:123], v[188:191], v[168:171], v[120:123]
	ds_read_b128 v[228:231], v13 offset:6144
	v_mfma_f32_16x16x32_bf16 v[124:127], v[188:191], v[172:175], v[124:127]
	global_load_lds_dwordx4 v6, s[18:19]
	v_mfma_f32_16x16x32_bf16 v[128:131], v[192:195], v[160:163], v[128:131]
	ds_read_b128 v[232:235], v13 offset:8192
	v_mfma_f32_16x16x32_bf16 v[132:135], v[192:195], v[164:167], v[132:135]
	s_add_u32 m0, s20, 0x9000
	v_mfma_f32_16x16x32_bf16 v[136:139], v[192:195], v[168:171], v[136:139]
	ds_read_b128 v[236:239], v13 offset:10240
	v_mfma_f32_16x16x32_bf16 v[140:143], v[192:195], v[172:175], v[140:143]
	global_load_lds_dwordx4 v7, s[18:19]
	v_mfma_f32_16x16x32_bf16 v[144:147], v[196:199], v[160:163], v[144:147]
	s_add_u32 s16, s16, 0x80
	s_addc_u32 s17, s17, 0
	s_add_u32 s18, s18, 0x80
	s_addc_u32 s19, s19, 0
	v_mfma_f32_16x16x32_bf16 v[148:151], v[196:199], v[164:167], v[148:151]
	s_add_u32 s20, s20, 0xa000
	s_sub_u32 s22, s20, 0x28000
	s_cmp_ge_u32 s20, 0x28000
	s_cselect_b32 s20, s22, s20
	v_mfma_f32_16x16x32_bf16 v[152:155], v[196:199], v[168:171], v[152:155]
	v_add_u32_e32 v10, s21, v8
	v_add_u32_e32 v12, s21, v9
	v_xor_b32_e32 v11, 64, v10
	v_xor_b32_e32 v13, 64, v12
	v_mfma_f32_16x16x32_bf16 v[156:159], v[196:199], v[172:175], v[156:159]
	s_add_u32 s21, s21, 0xa000
	s_sub_u32 s23, s21, 0x28000
	s_cmp_ge_u32 s21, 0x28000
	s_cselect_b32 s21, s23, s21
	s_waitcnt lgkmcnt(0)
	v_mfma_f32_16x16x32_bf16 v[64:67], v[216:219], v[200:203], v[64:67]
	v_mfma_f32_16x16x32_bf16 v[68:71], v[216:219], v[204:207], v[68:71]
	v_mfma_f32_16x16x32_bf16 v[72:75], v[216:219], v[208:211], v[72:75]
	v_mfma_f32_16x16x32_bf16 v[76:79], v[216:219], v[212:215], v[76:79]
	s_waitcnt vmcnt(20)
	s_barrier
	v_mfma_f32_16x16x32_bf16 v[80:83], v[220:223], v[200:203], v[80:83]
	ds_read_b128 v[160:163], v10 offset:0
	v_mfma_f32_16x16x32_bf16 v[84:87], v[220:223], v[204:207], v[84:87]
	s_add_u32 m0, s20, 0x0
	v_mfma_f32_16x16x32_bf16 v[88:91], v[220:223], v[208:211], v[88:91]
	ds_read_b128 v[164:167], v10 offset:2048
	v_mfma_f32_16x16x32_bf16 v[92:95], v[220:223], v[212:215], v[92:95]
	global_load_lds_dwordx4 v2, s[16:17]
	v_mfma_f32_16x16x32_bf16 v[96:99], v[224:227], v[200:203], v[96:99]
	ds_read_b128 v[168:171], v10 offset:4096
	v_mfma_f32_16x16x32_bf16 v[100:103], v[224:227], v[204:207], v[100:103]
	s_add_u32 m0, s20, 0x1000
	v_mfma_f32_16x16x32_bf16 v[104:107], v[224:227], v[208:211], v[104:107]
	ds_read_b128 v[172:175], v10 offset:6144
	v_mfma_f32_16x16x32_bf16 v[108:111], v[224:227], v[212:215], v[108:111]
	global_load_lds_dwordx4 v3, s[16:17]
	v_mfma_f32_16x16x32_bf16 v[112:115], v[228:231], v[200:203], v[112:115]
	ds_read_b128 v[176:179], v12 offset:0
	v_mfma_f32_16x16x32_bf16 v[116:119], v[228:231], v[204:207], v[116:119]
	s_add_u32 m0, s20, 0x2000
	v_mfma_f32_16x16x32_bf16 v[120:123], v[228:231], v[208:211], v[120:123]
	ds_read_b128 v[180:183], v12 offset:2048
	v_mfma_f32_16x16x32_bf16 v[124:127], v[228:231], v[212:215], v[124:127]
	global_load_lds_dwordx4 v4, s[16:17]
	v_mfma_f32_16x16x32_bf16 v[128:131], v[232:235], v[200:203], v[128:131]
	ds_read_b128 v[184:187], v12 offset:4096
	v_mfma_f32_16x16x32_bf16 v[132:135], v[232:235], v[204:207], v[132:135]
	s_add_u32 m0, s20, 0x3000
	v_mfma_f32_16x16x32_bf16 v[136:139], v[232:235], v[208:211], v[136:139]
	ds_read_b128 v[188:191], v12 offset:6144
	v_mfma_f32_16x16x32_bf16 v[140:143], v[232:235], v[212:215], v[140:143]
	global_load_lds_dwordx4 v5, s[16:17]
	v_mfma_f32_16x16x32_bf16 v[144:147], v[236:239], v[200:203], v[144:147]
	ds_read_b128 v[192:195], v12 offset:8192
	v_mfma_f32_16x16x32_bf16 v[148:151], v[236:239], v[204:207], v[148:151]
	s_add_u32 m0, s20, 0x4000
	v_mfma_f32_16x16x32_bf16 v[152:155], v[236:239], v[208:211], v[152:155]
	ds_read_b128 v[196:199], v12 offset:10240
	v_mfma_f32_16x16x32_bf16 v[156:159], v[236:239], v[212:215], v[156:159]
	global_load_lds_dwordx4 v2, s[18:19]
	s_add_u32 s15, s15, 1
	s_cmp_lt_u32 s15, 44
	s_cbranch_scc1 .Ldn_loop
	s_waitcnt lgkmcnt(0)
	v_mfma_f32_16x16x32_bf16 v[64:67], v[176:179], v[160:163], v[64:67]
	ds_read_b128 v[200:203], v11 offset:0
	v_mfma_f32_16x16x32_bf16 v[68:71], v[176:179], v[164:167], v[68:71]
	s_add_u32 m0, s20, 0x5000
	v_mfma_f32_16x16x32_bf16 v[72:75], v[176:179], v[168:171], v[72:75]
	ds_read_b128 v[204:207], v11 offset:2048
	v_mfma_f32_16x16x32_bf16 v[76:79], v[176:179], v[172:175], v[76:79]
	global_load_lds_dwordx4 v3, s[18:19]
	v_mfma_f32_16x16x32_bf16 v[80:83], v[180:183], v[160:163], v[80:83]
	ds_read_b128 v[208:211], v11 offset:4096
	v_mfma_f32_16x16x32_bf16 v[84:87], v[180:183], v[164:167], v[84:87]
	s_add_u32 m0, s20, 0x6000
	v_mfma_f32_16x16x32_bf16 v[88:91], v[180:183], v[168:171], v[88:91]
	ds_read_b128 v[212:215], v11 offset:6144
	v_mfma_f32_16x16x32_bf16 v[92:95], v[180:183], v[172:175], v[92:95]
	global_load_lds_dwordx4 v4, s[18:19]
	v_mfma_f32_16x16x32_bf16 v[96:99], v[184:187], v[160:163], v[96:99]
	ds_read_b128 v[216:219], v13 offset:0
	v_mfma_f32_16x16x32_bf16 v[100:103], v[184:187], v[164:167], v[100:103]
	s_add_u32 m0, s20, 0x7000
	v_mfma_f32_16x16x32_bf16 v[104:107], v[184:187], v[168:171], v[104:107]
	ds_read_b128 v[220:223], v13 offset:2048
	v_mfma_f32_16x16x32_bf16 v[108:111], v[184:187], v[172:175], v[108:111]
	global_load_lds_dwordx4 v5, s[18:19]
	v_mfma_f32_16x16x32_bf16 v[112:115], v[188:191], v[160:163], v[112:115]
	ds_read_b128 v[224:227], v13 offset:4096
	v_mfma_f32_16x16x32_bf16 v[116:119], v[188:191], v[164:167], v[116:119]
	s_add_u32 m0, s20, 0x8000
	v_mfma_f32_16x16x32_bf16 v[120:123], v[188:191], v[168:171], v[120:123]
	ds_read_b128 v[228:231], v13 offset:6144
	v_mfma_f32_16x16x32_bf16 v[124:127], v[188:191], v[172:175], v[124:127]
	global_load_lds_dwordx4 v6, s[18:19]
	v_mfma_f32_16x16x32_bf16 v[128:131], v[192:195], v[160:163], v[128:131]
	ds_read_b128 v[232:235], v13 offset:8192
	v_mfma_f32_16x16x32_bf16 v[132:135], v[192:195], v[164:167], v[132:135]
	s_add_u32 m0, s20, 0x9000
	v_mfma_f32_16x16x32_bf16 v[136:139], v[192:195], v[168:171], v[136:139]
	ds_read_b128 v[236:239], v13 offset:10240
	v_mfma_f32_16x16x32_bf16 v[140:143], v[192:195], v[172:175], v[140:143]
	global_load_lds_dwordx4 v7, s[18:19]
	v_mfma_f32_16x16x32_bf16 v[144:147], v[196:199], v[160:163], v[144:147]
	s_add_u32 s16, s16, 0x80
	s_addc_u32 s17, s17, 0
	s_add_u32 s18, s18, 0x80
	s_addc_u32 s19, s19, 0
	v_mfma_f32_16x16x32_bf16 v[148:151], v[196:199], v[164:167], v[148:151]
	s_add_u32 s20, s20, 0xa000
	s_sub_u32 s22, s20, 0x28000
	s_cmp_ge_u32 s20, 0x28000
	s_cselect_b32 s20, s22, s20
	v_mfma_f32_16x16x32_bf16 v[152:155], v[196:199], v[168:171], v[152:155]
	v_add_u32_e32 v10, s21, v8
	v_add_u32_e32 v12, s21, v9
	v_xor_b32_e32 v11, 64, v10
	v_xor_b32_e32 v13, 64, v12
	v_mfma_f32_16x16x32_bf16 v[156:159], v[196:199], v[172:175], v[156:159]
	s_add_u32 s21, s21, 0xa000
	s_sub_u32 s23, s21, 0x28000
	s_cmp_ge_u32 s21, 0x28000
	s_cselect_b32 s21, s23, s21
	s_waitcnt lgkmcnt(0)
	v_mfma_f32_16x16x32_bf16 v[64:67], v[216:219], v[200:203], v[64:67]
	v_mfma_f32_16x16x32_bf16 v[68:71], v[216:219], v[204:207], v[68:71]
	v_mfma_f32_16x16x32_bf16 v[72:75], v[216:219], v[208:211], v[72:75]
	v_mfma_f32_16x16x32_bf16 v[76:79], v[216:219], v[212:215], v[76:79]
	s_waitcnt vmcnt(20)
	s_barrier
	v_mfma_f32_16x16x32_bf16 v[80:83], v[220:223], v[200:203], v[80:83]
	ds_read_b128 v[160:163], v10 offset:0
	v_mfma_f32_16x16x32_bf16 v[84:87], v[220:223], v[204:207], v[84:87]
	global_load_dwordx4 v[16:19], v56, s[8:9] offset:0
	v_mfma_f32_16x16x32_bf16 v[88:91], v[220:223], v[208:211], v[88:91]
	ds_read_b128 v[164:167], v10 offset:2048
	v_mfma_f32_16x16x32_bf16 v[92:95], v[220:223], v[212:215], v[92:95]
	global_load_dwordx4 v[20:23], v57, s[8:9] offset:0
	v_mfma_f32_16x16x32_bf16 v[96:99], v[224:227], v[200:203], v[96:99]
	ds_read_b128 v[168:171], v10 offset:4096
	v_mfma_f32_16x16x32_bf16 v[100:103], v[224:227], v[204:207], v[100:103]
	global_load_dwordx4 v[24:27], v58, s[8:9] offset:0
	v_mfma_f32_16x16x32_bf16 v[104:107], v[224:227], v[208:211], v[104:107]
	ds_read_b128 v[172:175], v10 offset:6144
	v_mfma_f32_16x16x32_bf16 v[108:111], v[224:227], v[212:215], v[108:111]
	global_load_dwordx4 v[28:31], v59, s[8:9] offset:0
	v_mfma_f32_16x16x32_bf16 v[112:115], v[228:231], v[200:203], v[112:115]
	ds_read_b128 v[176:179], v12 offset:0
	v_mfma_f32_16x16x32_bf16 v[116:119], v[228:231], v[204:207], v[116:119]
	global_load_dwordx4 v[32:35], v56, s[8:9] offset:64
	v_mfma_f32_16x16x32_bf16 v[120:123], v[228:231], v[208:211], v[120:123]
	ds_read_b128 v[180:183], v12 offset:2048
	v_mfma_f32_16x16x32_bf16 v[124:127], v[228:231], v[212:215], v[124:127]
	global_load_dwordx4 v[36:39], v57, s[8:9] offset:64
	v_mfma_f32_16x16x32_bf16 v[128:131], v[232:235], v[200:203], v[128:131]
	ds_read_b128 v[184:187], v12 offset:4096
	v_mfma_f32_16x16x32_bf16 v[132:135], v[232:235], v[204:207], v[132:135]
	global_load_dwordx4 v[40:43], v58, s[8:9] offset:64
	v_mfma_f32_16x16x32_bf16 v[136:139], v[232:235], v[208:211], v[136:139]
	ds_read_b128 v[188:191], v12 offset:6144
	v_mfma_f32_16x16x32_bf16 v[140:143], v[232:235], v[212:215], v[140:143]
	global_load_dwordx4 v[44:47], v59, s[8:9] offset:64
	v_mfma_f32_16x16x32_bf16 v[144:147], v[236:239], v[200:203], v[144:147]
	ds_read_b128 v[192:195], v12 offset:8192
	v_mfma_f32_16x16x32_bf16 v[148:151], v[236:239], v[204:207], v[148:151]
	global_load_dwordx4 v[48:51], v56, s[8:9] offset:128
	v_mfma_f32_16x16x32_bf16 v[152:155], v[236:239], v[208:211], v[152:155]
	ds_read_b128 v[196:199], v12 offset:10240
	v_mfma_f32_16x16x32_bf16 v[156:159], v[236:239], v[212:215], v[156:159]
	global_load_dwordx4 v[52:55], v57, s[8:9] offset:128
	global_load_dwordx4 v[240:243], v58, s[8:9] offset:128
	global_load_dwordx4 v[244:247], v59, s[8:9] offset:128
	global_load_dwordx4 v[248:251], v56, s[8:9] offset:192
	global_load_dwordx4 v[252:255], v57, s[8:9] offset:192
	s_waitcnt lgkmcnt(0)
	v_mfma_f32_16x16x32_bf16 v[64:67], v[176:179], v[160:163], v[64:67]
	ds_read_b128 v[200:203], v11 offset:0
	v_mfma_f32_16x16x32_bf16 v[68:71], v[176:179], v[164:167], v[68:71]
	ds_read_b128 v[204:207], v11 offset:2048
	v_mfma_f32_16x16x32_bf16 v[72:75], v[176:179], v[168:171], v[72:75]
	ds_read_b128 v[208:211], v11 offset:4096
	v_mfma_f32_16x16x32_bf16 v[76:79], v[176:179], v[172:175], v[76:79]
	ds_read_b128 v[212:215], v11 offset:6144
	v_mfma_f32_16x16x32_bf16 v[80:83], v[180:183], v[160:163], v[80:83]
	ds_read_b128 v[216:219], v13 offset:0
	v_mfma_f32_16x16x32_bf16 v[84:87], v[180:183], v[164:167], v[84:87]
	ds_read_b128 v[220:223], v13 offset:2048
	v_mfma_f32_16x16x32_bf16 v[88:91], v[180:183], v[168:171], v[88:91]
	ds_read_b128 v[224:227], v13 offset:4096
	v_mfma_f32_16x16x32_bf16 v[92:95], v[180:183], v[172:175], v[92:95]
	ds_read_b128 v[228:231], v13 offset:6144
	v_mfma_f32_16x16x32_bf16 v[96:99], v[184:187], v[160:163], v[96:99]
	ds_read_b128 v[232:235], v13 offset:8192
	v_mfma_f32_16x16x32_bf16 v[100:103], v[184:187], v[164:167], v[100:103]
	ds_read_b128 v[236:239], v13 offset:10240
	v_mfma_f32_16x16x32_bf16 v[104:107], v[184:187], v[168:171], v[104:107]
	v_mfma_f32_16x16x32_bf16 v[108:111], v[184:187], v[172:175], v[108:111]
	v_mfma_f32_16x16x32_bf16 v[112:115], v[188:191], v[160:163], v[112:115]
	v_mfma_f32_16x16x32_bf16 v[116:119], v[188:191], v[164:167], v[116:119]
	v_mfma_f32_16x16x32_bf16 v[120:123], v[188:191], v[168:171], v[120:123]
	v_mfma_f32_16x16x32_bf16 v[124:127], v[188:191], v[172:175], v[124:127]
	v_mfma_f32_16x16x32_bf16 v[128:131], v[192:195], v[160:163], v[128:131]
	v_mfma_f32_16x16x32_bf16 v[132:135], v[192:195], v[164:167], v[132:135]
	v_mfma_f32_16x16x32_bf16 v[136:139], v[192:195], v[168:171], v[136:139]
	v_mfma_f32_16x16x32_bf16 v[140:143], v[192:195], v[172:175], v[140:143]
	v_mfma_f32_16x16x32_bf16 v[144:147], v[196:199], v[160:163], v[144:147]
	v_add_u32_e32 v10, s21, v8
	v_add_u32_e32 v12, s21, v9
	v_xor_b32_e32 v11, 64, v10
	v_xor_b32_e32 v13, 64, v12
	v_mfma_f32_16x16x32_bf16 v[148:151], v[196:199], v[164:167], v[148:151]
	s_add_u32 s21, s21, 0xa000
	s_sub_u32 s23, s21, 0x28000
	s_cmp_ge_u32 s21, 0x28000
	s_cselect_b32 s21, s23, s21
	v_mfma_f32_16x16x32_bf16 v[152:155], v[196:199], v[168:171], v[152:155]
	v_mfma_f32_16x16x32_bf16 v[156:159], v[196:199], v[172:175], v[156:159]
	s_waitcnt lgkmcnt(0)
	v_mfma_f32_16x16x32_bf16 v[64:67], v[216:219], v[200:203], v[64:67]
	v_mfma_f32_16x16x32_bf16 v[68:71], v[216:219], v[204:207], v[68:71]
	v_mfma_f32_16x16x32_bf16 v[72:75], v[216:219], v[208:211], v[72:75]
	v_mfma_f32_16x16x32_bf16 v[76:79], v[216:219], v[212:215], v[76:79]
	s_waitcnt vmcnt(24)
	s_barrier
	v_mfma_f32_16x16x32_bf16 v[80:83], v[220:223], v[200:203], v[80:83]
	ds_read_b128 v[160:163], v10 offset:0
	v_mfma_f32_16x16x32_bf16 v[84:87], v[220:223], v[204:207], v[84:87]
	ds_read_b128 v[164:167], v10 offset:2048
	v_mfma_f32_16x16x32_bf16 v[88:91], v[220:223], v[208:211], v[88:91]
	ds_read_b128 v[168:171], v10 offset:4096
	v_mfma_f32_16x16x32_bf16 v[92:95], v[220:223], v[212:215], v[92:95]
	ds_read_b128 v[172:175], v10 offset:6144
	v_mfma_f32_16x16x32_bf16 v[96:99], v[224:227], v[200:203], v[96:99]
	ds_read_b128 v[176:179], v12 offset:0
	v_mfma_f32_16x16x32_bf16 v[100:103], v[224:227], v[204:207], v[100:103]
	ds_read_b128 v[180:183], v12 offset:2048
	v_mfma_f32_16x16x32_bf16 v[104:107], v[224:227], v[208:211], v[104:107]
	ds_read_b128 v[184:187], v12 offset:4096
	v_mfma_f32_16x16x32_bf16 v[108:111], v[224:227], v[212:215], v[108:111]
	ds_read_b128 v[188:191], v12 offset:6144
	v_mfma_f32_16x16x32_bf16 v[112:115], v[228:231], v[200:203], v[112:115]
	ds_read_b128 v[192:195], v12 offset:8192
	v_mfma_f32_16x16x32_bf16 v[116:119], v[228:231], v[204:207], v[116:119]
	ds_read_b128 v[196:199], v12 offset:10240
	v_mfma_f32_16x16x32_bf16 v[120:123], v[228:231], v[208:211], v[120:123]
	v_mfma_f32_16x16x32_bf16 v[124:127], v[228:231], v[212:215], v[124:127]
	v_mfma_f32_16x16x32_bf16 v[128:131], v[232:235], v[200:203], v[128:131]
	v_mfma_f32_16x16x32_bf16 v[132:135], v[232:235], v[204:207], v[132:135]
	v_mfma_f32_16x16x32_bf16 v[136:139], v[232:235], v[208:211], v[136:139]
	v_mfma_f32_16x16x32_bf16 v[140:143], v[232:235], v[212:215], v[140:143]
	v_mfma_f32_16x16x32_bf16 v[144:147], v[236:239], v[200:203], v[144:147]
	v_mfma_f32_16x16x32_bf16 v[148:151], v[236:239], v[204:207], v[148:151]
	v_mfma_f32_16x16x32_bf16 v[152:155], v[236:239], v[208:211], v[152:155]
	v_mfma_f32_16x16x32_bf16 v[156:159], v[236:239], v[212:215], v[156:159]
	s_waitcnt lgkmcnt(0)
	v_mfma_f32_16x16x32_bf16 v[64:67], v[176:179], v[160:163], v[64:67]
	ds_read_b128 v[200:203], v11 offset:0
	v_mfma_f32_16x16x32_bf16 v[68:71], v[176:179], v[164:167], v[68:71]
	ds_read_b128 v[204:207], v11 offset:2048
	v_mfma_f32_16x16x32_bf16 v[72:75], v[176:179], v[168:171], v[72:75]
	ds_read_b128 v[208:211], v11 offset:4096
	v_mfma_f32_16x16x32_bf16 v[76:79], v[176:179], v[172:175], v[76:79]
	ds_read_b128 v[212:215], v11 offset:6144
	v_mfma_f32_16x16x32_bf16 v[80:83], v[180:183], v[160:163], v[80:83]
	ds_read_b128 v[216:219], v13 offset:0
	v_mfma_f32_16x16x32_bf16 v[84:87], v[180:183], v[164:167], v[84:87]
	ds_read_b128 v[220:223], v13 offset:2048
	v_mfma_f32_16x16x32_bf16 v[88:91], v[180:183], v[168:171], v[88:91]
	ds_read_b128 v[224:227], v13 offset:4096
	v_mfma_f32_16x16x32_bf16 v[92:95], v[180:183], v[172:175], v[92:95]
	ds_read_b128 v[228:231], v13 offset:6144
	v_mfma_f32_16x16x32_bf16 v[96:99], v[184:187], v[160:163], v[96:99]
	ds_read_b128 v[232:235], v13 offset:8192
	v_mfma_f32_16x16x32_bf16 v[100:103], v[184:187], v[164:167], v[100:103]
	ds_read_b128 v[236:239], v13 offset:10240
	v_mfma_f32_16x16x32_bf16 v[104:107], v[184:187], v[168:171], v[104:107]
	v_mfma_f32_16x16x32_bf16 v[108:111], v[184:187], v[172:175], v[108:111]
	v_mfma_f32_16x16x32_bf16 v[112:115], v[188:191], v[160:163], v[112:115]
	v_mfma_f32_16x16x32_bf16 v[116:119], v[188:191], v[164:167], v[116:119]
	v_mfma_f32_16x16x32_bf16 v[120:123], v[188:191], v[168:171], v[120:123]
	v_mfma_f32_16x16x32_bf16 v[124:127], v[188:191], v[172:175], v[124:127]
	v_mfma_f32_16x16x32_bf16 v[128:131], v[192:195], v[160:163], v[128:131]
	v_mfma_f32_16x16x32_bf16 v[132:135], v[192:195], v[164:167], v[132:135]
	v_mfma_f32_16x16x32_bf16 v[136:139], v[192:195], v[168:171], v[136:139]
	v_mfma_f32_16x16x32_bf16 v[140:143], v[192:195], v[172:175], v[140:143]
	v_mfma_f32_16x16x32_bf16 v[144:147], v[196:199], v[160:163], v[144:147]
	v_add_u32_e32 v10, s21, v8
	v_add_u32_e32 v12, s21, v9
	v_xor_b32_e32 v11, 64, v10
	v_xor_b32_e32 v13, 64, v12
	v_mfma_f32_16x16x32_bf16 v[148:151], v[196:199], v[164:167], v[148:151]
	s_add_u32 s21, s21, 0xa000
	s_sub_u32 s23, s21, 0x28000
	s_cmp_ge_u32 s21, 0x28000
	s_cselect_b32 s21, s23, s21
	v_mfma_f32_16x16x32_bf16 v[152:155], v[196:199], v[168:171], v[152:155]
	v_mfma_f32_16x16x32_bf16 v[156:159], v[196:199], v[172:175], v[156:159]
	s_waitcnt lgkmcnt(0)
	v_mfma_f32_16x16x32_bf16 v[64:67], v[216:219], v[200:203], v[64:67]
	v_mfma_f32_16x16x32_bf16 v[68:71], v[216:219], v[204:207], v[68:71]
	v_mfma_f32_16x16x32_bf16 v[72:75], v[216:219], v[208:211], v[72:75]
	v_mfma_f32_16x16x32_bf16 v[76:79], v[216:219], v[212:215], v[76:79]
	s_waitcnt vmcnt(14)
	s_barrier
	v_mfma_f32_16x16x32_bf16 v[80:83], v[220:223], v[200:203], v[80:83]
	ds_read_b128 v[160:163], v10 offset:0
	v_mfma_f32_16x16x32_bf16 v[84:87], v[220:223], v[204:207], v[84:87]
	ds_read_b128 v[164:167], v10 offset:2048
	v_mfma_f32_16x16x32_bf16 v[88:91], v[220:223], v[208:211], v[88:91]
	ds_read_b128 v[168:171], v10 offset:4096
	v_mfma_f32_16x16x32_bf16 v[92:95], v[220:223], v[212:215], v[92:95]
	ds_read_b128 v[172:175], v10 offset:6144
	v_mfma_f32_16x16x32_bf16 v[96:99], v[224:227], v[200:203], v[96:99]
	ds_read_b128 v[176:179], v12 offset:0
	v_mfma_f32_16x16x32_bf16 v[100:103], v[224:227], v[204:207], v[100:103]
	ds_read_b128 v[180:183], v12 offset:2048
	v_mfma_f32_16x16x32_bf16 v[104:107], v[224:227], v[208:211], v[104:107]
	ds_read_b128 v[184:187], v12 offset:4096
	v_mfma_f32_16x16x32_bf16 v[108:111], v[224:227], v[212:215], v[108:111]
	ds_read_b128 v[188:191], v12 offset:6144
	v_mfma_f32_16x16x32_bf16 v[112:115], v[228:231], v[200:203], v[112:115]
	ds_read_b128 v[192:195], v12 offset:8192
	v_mfma_f32_16x16x32_bf16 v[116:119], v[228:231], v[204:207], v[116:119]
	ds_read_b128 v[196:199], v12 offset:10240
	v_mfma_f32_16x16x32_bf16 v[120:123], v[228:231], v[208:211], v[120:123]
	v_mfma_f32_16x16x32_bf16 v[124:127], v[228:231], v[212:215], v[124:127]
	v_mfma_f32_16x16x32_bf16 v[128:131], v[232:235], v[200:203], v[128:131]
	v_mfma_f32_16x16x32_bf16 v[132:135], v[232:235], v[204:207], v[132:135]
	v_mfma_f32_16x16x32_bf16 v[136:139], v[232:235], v[208:211], v[136:139]
	v_mfma_f32_16x16x32_bf16 v[140:143], v[232:235], v[212:215], v[140:143]
	v_mfma_f32_16x16x32_bf16 v[144:147], v[236:239], v[200:203], v[144:147]
	v_mfma_f32_16x16x32_bf16 v[148:151], v[236:239], v[204:207], v[148:151]
	v_mfma_f32_16x16x32_bf16 v[152:155], v[236:239], v[208:211], v[152:155]
	v_mfma_f32_16x16x32_bf16 v[156:159], v[236:239], v[212:215], v[156:159]
	s_waitcnt lgkmcnt(0)
	v_mfma_f32_16x16x32_bf16 v[64:67], v[176:179], v[160:163], v[64:67]
	ds_read_b128 v[200:203], v11 offset:0
	v_mfma_f32_16x16x32_bf16 v[68:71], v[176:179], v[164:167], v[68:71]
	ds_read_b128 v[204:207], v11 offset:2048
	v_mfma_f32_16x16x32_bf16 v[72:75], v[176:179], v[168:171], v[72:75]
	ds_read_b128 v[208:211], v11 offset:4096
	v_mfma_f32_16x16x32_bf16 v[76:79], v[176:179], v[172:175], v[76:79]
	ds_read_b128 v[212:215], v11 offset:6144
	v_mfma_f32_16x16x32_bf16 v[80:83], v[180:183], v[160:163], v[80:83]
	ds_read_b128 v[216:219], v13 offset:0
	v_mfma_f32_16x16x32_bf16 v[84:87], v[180:183], v[164:167], v[84:87]
	ds_read_b128 v[220:223], v13 offset:2048
	v_mfma_f32_16x16x32_bf16 v[88:91], v[180:183], v[168:171], v[88:91]
	ds_read_b128 v[224:227], v13 offset:4096
	v_mfma_f32_16x16x32_bf16 v[92:95], v[180:183], v[172:175], v[92:95]
	ds_read_b128 v[228:231], v13 offset:6144
	v_mfma_f32_16x16x32_bf16 v[96:99], v[184:187], v[160:163], v[96:99]
	ds_read_b128 v[232:235], v13 offset:8192
	v_mfma_f32_16x16x32_bf16 v[100:103], v[184:187], v[164:167], v[100:103]
	ds_read_b128 v[236:239], v13 offset:10240
	v_mfma_f32_16x16x32_bf16 v[104:107], v[184:187], v[168:171], v[104:107]
	v_mfma_f32_16x16x32_bf16 v[108:111], v[184:187], v[172:175], v[108:111]
	v_mfma_f32_16x16x32_bf16 v[112:115], v[188:191], v[160:163], v[112:115]
	v_mfma_f32_16x16x32_bf16 v[116:119], v[188:191], v[164:167], v[116:119]
	v_mfma_f32_16x16x32_bf16 v[120:123], v[188:191], v[168:171], v[120:123]
	v_mfma_f32_16x16x32_bf16 v[124:127], v[188:191], v[172:175], v[124:127]
	v_mfma_f32_16x16x32_bf16 v[128:131], v[192:195], v[160:163], v[128:131]
	v_mfma_f32_16x16x32_bf16 v[132:135], v[192:195], v[164:167], v[132:135]
	v_mfma_f32_16x16x32_bf16 v[136:139], v[192:195], v[168:171], v[136:139]
	v_mfma_f32_16x16x32_bf16 v[140:143], v[192:195], v[172:175], v[140:143]
	v_mfma_f32_16x16x32_bf16 v[144:147], v[196:199], v[160:163], v[144:147]
	v_mfma_f32_16x16x32_bf16 v[148:151], v[196:199], v[164:167], v[148:151]
	v_mfma_f32_16x16x32_bf16 v[152:155], v[196:199], v[168:171], v[152:155]
	v_mfma_f32_16x16x32_bf16 v[156:159], v[196:199], v[172:175], v[156:159]
	s_waitcnt lgkmcnt(0)
	v_mfma_f32_16x16x32_bf16 v[64:67], v[216:219], v[200:203], v[64:67]
	v_mfma_f32_16x16x32_bf16 v[68:71], v[216:219], v[204:207], v[68:71]
	global_load_dwordx4 v[160:163], v58, s[8:9] offset:192
	v_mfma_f32_16x16x32_bf16 v[72:75], v[216:219], v[208:211], v[72:75]
	v_mfma_f32_16x16x32_bf16 v[76:79], v[216:219], v[212:215], v[76:79]
	global_load_dwordx4 v[164:167], v59, s[8:9] offset:192
	v_mfma_f32_16x16x32_bf16 v[80:83], v[220:223], v[200:203], v[80:83]
	v_mfma_f32_16x16x32_bf16 v[84:87], v[220:223], v[204:207], v[84:87]
	global_load_dwordx4 v[168:171], v56, s[8:9] offset:256
	v_mfma_f32_16x16x32_bf16 v[88:91], v[220:223], v[208:211], v[88:91]
	v_mfma_f32_16x16x32_bf16 v[92:95], v[220:223], v[212:215], v[92:95]
	global_load_dwordx4 v[172:175], v57, s[8:9] offset:256
	v_mfma_f32_16x16x32_bf16 v[96:99], v[224:227], v[200:203], v[96:99]
	v_mfma_f32_16x16x32_bf16 v[100:103], v[224:227], v[204:207], v[100:103]
	global_load_dwordx4 v[176:179], v58, s[8:9] offset:256
	v_mfma_f32_16x16x32_bf16 v[104:107], v[224:227], v[208:211], v[104:107]
	v_mfma_f32_16x16x32_bf16 v[108:111], v[224:227], v[212:215], v[108:111]
	global_load_dwordx4 v[180:183], v59, s[8:9] offset:256
	v_mfma_f32_16x16x32_bf16 v[112:115], v[228:231], v[200:203], v[112:115]
	v_mfma_f32_16x16x32_bf16 v[116:119], v[228:231], v[204:207], v[116:119]
	global_load_dwordx4 v[184:187], v56, s[8:9] offset:320
	v_mfma_f32_16x16x32_bf16 v[120:123], v[228:231], v[208:211], v[120:123]
	v_mfma_f32_16x16x32_bf16 v[124:127], v[228:231], v[212:215], v[124:127]
	global_load_dwordx4 v[188:191], v57, s[8:9] offset:320
	v_mfma_f32_16x16x32_bf16 v[128:131], v[232:235], v[200:203], v[128:131]
	v_mfma_f32_16x16x32_bf16 v[132:135], v[232:235], v[204:207], v[132:135]
	global_load_dwordx4 v[192:195], v58, s[8:9] offset:320
	v_mfma_f32_16x16x32_bf16 v[136:139], v[232:235], v[208:211], v[136:139]
	v_mfma_f32_16x16x32_bf16 v[140:143], v[232:235], v[212:215], v[140:143]
	global_load_dwordx4 v[196:199], v59, s[8:9] offset:320
	v_mfma_f32_16x16x32_bf16 v[144:147], v[236:239], v[200:203], v[144:147]
	v_mfma_f32_16x16x32_bf16 v[148:151], v[236:239], v[204:207], v[148:151]
	v_mfma_f32_16x16x32_bf16 v[152:155], v[236:239], v[208:211], v[152:155]
	v_mfma_f32_16x16x32_bf16 v[156:159], v[236:239], v[212:215], v[156:159]
	s_waitcnt vmcnt(23)
	v_pk_add_f32 v[64:65], v[64:65], v[16:17]
	v_pk_add_f32 v[66:67], v[66:67], v[18:19]
	global_store_dwordx4 v56, v[64:67], s[10:11] offset:0
	s_waitcnt vmcnt(23)
	v_pk_add_f32 v[68:69], v[68:69], v[20:21]
	v_pk_add_f32 v[70:71], v[70:71], v[22:23]
	global_store_dwordx4 v57, v[68:71], s[10:11] offset:0
	s_waitcnt vmcnt(23)
	v_pk_add_f32 v[72:73], v[72:73], v[24:25]
	v_pk_add_f32 v[74:75], v[74:75], v[26:27]
	global_store_dwordx4 v58, v[72:75], s[10:11] offset:0
	s_waitcnt vmcnt(23)
	v_pk_add_f32 v[76:77], v[76:77], v[28:29]
	v_pk_add_f32 v[78:79], v[78:79], v[30:31]
	global_store_dwordx4 v59, v[76:79], s[10:11] offset:0
	s_waitcnt vmcnt(23)
	v_pk_add_f32 v[80:81], v[80:81], v[32:33]
	v_pk_add_f32 v[82:83], v[82:83], v[34:35]
	global_store_dwordx4 v56, v[80:83], s[10:11] offset:64
	s_waitcnt vmcnt(23)
	v_pk_add_f32 v[84:85], v[84:85], v[36:37]
	v_pk_add_f32 v[86:87], v[86:87], v[38:39]
	global_store_dwordx4 v57, v[84:87], s[10:11] offset:64
	s_waitcnt vmcnt(23)
	v_pk_add_f32 v[88:89], v[88:89], v[40:41]
	v_pk_add_f32 v[90:91], v[90:91], v[42:43]
	global_store_dwordx4 v58, v[88:91], s[10:11] offset:64
	s_waitcnt vmcnt(23)
	v_pk_add_f32 v[92:93], v[92:93], v[44:45]
	v_pk_add_f32 v[94:95], v[94:95], v[46:47]
	global_store_dwordx4 v59, v[92:95], s[10:11] offset:64
	s_waitcnt vmcnt(23)
	v_pk_add_f32 v[96:97], v[96:97], v[48:49]
	v_pk_add_f32 v[98:99], v[98:99], v[50:51]
	global_store_dwordx4 v56, v[96:99], s[10:11] offset:128
	s_waitcnt vmcnt(23)
	v_pk_add_f32 v[100:101], v[100:101], v[52:53]
	v_pk_add_f32 v[102:103], v[102:103], v[54:55]
	global_store_dwordx4 v57, v[100:103], s[10:11] offset:128
	s_waitcnt vmcnt(23)
	v_pk_add_f32 v[104:105], v[104:105], v[240:241]
	v_pk_add_f32 v[106:107], v[106:107], v[242:243]
	global_store_dwordx4 v58, v[104:107], s[10:11] offset:128
	s_waitcnt vmcnt(23)
	v_pk_add_f32 v[108:109], v[108:109], v[244:245]
	v_pk_add_f32 v[110:111], v[110:111], v[246:247]
	global_store_dwordx4 v59, v[108:111], s[10:11] offset:128
	s_waitcnt vmcnt(23)
	v_pk_add_f32 v[112:113], v[112:113], v[248:249]
	v_pk_add_f32 v[114:115], v[114:115], v[250:251]
	global_store_dwordx4 v56, v[112:115], s[10:11] offset:192
	s_waitcnt vmcnt(23)
	v_pk_add_f32 v[116:117], v[116:117], v[252:253]
	v_pk_add_f32 v[118:119], v[118:119], v[254:255]
	global_store_dwordx4 v57, v[116:119], s[10:11] offset:192
	s_waitcnt vmcnt(23)
	v_pk_add_f32 v[120:121], v[120:121], v[160:161]
	v_pk_add_f32 v[122:123], v[122:123], v[162:163]
	global_store_dwordx4 v58, v[120:123], s[10:11] offset:192
	s_waitcnt vmcnt(23)
	v_pk_add_f32 v[124:125], v[124:125], v[164:165]
	v_pk_add_f32 v[126:127], v[126:127], v[166:167]
	global_store_dwordx4 v59, v[124:127], s[10:11] offset:192
	s_waitcnt vmcnt(23)
	v_pk_add_f32 v[128:129], v[128:129], v[168:169]
	v_pk_add_f32 v[130:131], v[130:131], v[170:171]
	global_store_dwordx4 v56, v[128:131], s[10:11] offset:256
	s_waitcnt vmcnt(23)
	v_pk_add_f32 v[132:133], v[132:133], v[172:173]
	v_pk_add_f32 v[134:135], v[134:135], v[174:175]
	global_store_dwordx4 v57, v[132:135], s[10:11] offset:256
	s_waitcnt vmcnt(23)
	v_pk_add_f32 v[136:137], v[136:137], v[176:177]
	v_pk_add_f32 v[138:139], v[138:139], v[178:179]
	global_store_dwordx4 v58, v[136:139], s[10:11] offset:256
	s_waitcnt vmcnt(23)
	v_pk_add_f32 v[140:141], v[140:141], v[180:181]
	v_pk_add_f32 v[142:143], v[142:143], v[182:183]
	global_store_dwordx4 v59, v[140:143], s[10:11] offset:256
	s_waitcnt vmcnt(23)
	v_pk_add_f32 v[144:145], v[144:145], v[184:185]
	v_pk_add_f32 v[146:147], v[146:147], v[186:187]
	global_store_dwordx4 v56, v[144:147], s[10:11] offset:320
	s_waitcnt vmcnt(23)
	v_pk_add_f32 v[148:149], v[148:149], v[188:189]
	v_pk_add_f32 v[150:151], v[150:151], v[190:191]
	global_store_dwordx4 v57, v[148:151], s[10:11] offset:320
	s_waitcnt vmcnt(23)
	v_pk_add_f32 v[152:153], v[152:153], v[192:193]
	v_pk_add_f32 v[154:155], v[154:155], v[194:195]
	global_store_dwordx4 v58, v[152:155], s[10:11] offset:320
	s_waitcnt vmcnt(23)
	v_pk_add_f32 v[156:157], v[156:157], v[196:197]
	v_pk_add_f32 v[158:159], v[158:159], v[198:199]
	global_store_dwordx4 v59, v[156:159], s[10:11] offset:320
